# P4: skinny meta epilogue loads issued together; tile epilogue rewritten with two residual row batches in flight
# speedup vs baseline: 1.0034x; 1.0018x over previous
.LBB0_817:
	v_add_u32_e32 v12, s6, v222
	v_ashrrev_i32_e32 v13, 31, v12
	v_lshlrev_b64 v[12:13], 11, v[12:13]
	v_lshl_add_u64 v[56:57], v[4:5], 0, v[12:13]
	v_add_co_u32_e32 v58, vcc, 0x8000, v56
	global_load_dwordx4 v[12:15], v[56:57], off
	global_load_dwordx4 v[16:19], v[2:3], off
	v_addc_co_u32_e32 v59, vcc, 0, v57, vcc
	v_add_co_u32_e32 v60, vcc, 0x10000, v56
	global_load_dwordx4 v[20:23], v[58:59], off
	s_nop 0
	v_addc_co_u32_e32 v61, vcc, 0, v57, vcc
	v_add_co_u32_e32 v62, vcc, 0x18000, v56
	global_load_dwordx4 v[24:27], v[60:61], off
	s_nop 0
	v_addc_co_u32_e32 v63, vcc, 0, v57, vcc
	global_load_dwordx4 v[28:31], v[62:63], off
	global_load_dwordx4 v[32:35], v[56:57], off offset:64
	global_load_dwordx4 v[36:39], v[2:3], off offset:64
	global_load_dwordx4 v[40:43], v[58:59], off offset:64
	global_load_dwordx4 v[44:47], v[60:61], off offset:64
	global_load_dwordx4 v[48:51], v[62:63], off offset:64
	s_and_b64 vcc, exec, s[4:5]
	s_waitcnt vmcnt(8)
	v_mfma_f32_16x16x32_bf16 v[12:15], v[12:15], v[16:19], 0
	s_waitcnt vmcnt(7)
	v_mfma_f32_16x16x32_bf16 v[20:23], v[20:23], v[16:19], 0
	s_waitcnt vmcnt(6)
	v_mfma_f32_16x16x32_bf16 v[24:27], v[24:27], v[16:19], 0
	s_waitcnt vmcnt(5)
	v_mfma_f32_16x16x32_bf16 v[16:19], v[28:31], v[16:19], 0
	global_load_dwordx4 v[28:31], v[56:57], off offset:128
	global_load_dwordx4 v[52:55], v[2:3], off offset:128
	s_waitcnt vmcnt(5)
	v_mfma_f32_16x16x32_bf16 v[12:15], v[32:35], v[36:39], v[12:15]
	global_load_dwordx4 v[32:35], v[58:59], off offset:128
	s_waitcnt vmcnt(5)
	v_mfma_f32_16x16x32_bf16 v[20:23], v[40:43], v[36:39], v[20:23]
	global_load_dwordx4 v[40:43], v[60:61], off offset:128
	s_waitcnt vmcnt(5)
	v_mfma_f32_16x16x32_bf16 v[24:27], v[44:47], v[36:39], v[24:27]
	global_load_dwordx4 v[44:47], v[62:63], off offset:128
	s_waitcnt vmcnt(5)
	v_mfma_f32_16x16x32_bf16 v[16:19], v[48:51], v[36:39], v[16:19]
	global_load_dwordx4 v[36:39], v[56:57], off offset:192
	global_load_dwordx4 v[48:51], v[2:3], off offset:192
	s_waitcnt vmcnt(5)
	v_mfma_f32_16x16x32_bf16 v[12:15], v[28:31], v[52:55], v[12:15]
	global_load_dwordx4 v[28:31], v[58:59], off offset:192
	s_waitcnt vmcnt(5)
	v_mfma_f32_16x16x32_bf16 v[20:23], v[32:35], v[52:55], v[20:23]
	global_load_dwordx4 v[32:35], v[60:61], off offset:192
	s_waitcnt vmcnt(5)
	v_mfma_f32_16x16x32_bf16 v[24:27], v[40:43], v[52:55], v[24:27]
	global_load_dwordx4 v[40:43], v[62:63], off offset:192
	s_barrier
	s_waitcnt vmcnt(5)
	v_mfma_f32_16x16x32_bf16 v[16:19], v[44:47], v[52:55], v[16:19]
	s_waitcnt vmcnt(3)
	v_mfma_f32_16x16x32_bf16 v[12:15], v[36:39], v[48:51], v[12:15]
	s_waitcnt vmcnt(2)
	v_mfma_f32_16x16x32_bf16 v[20:23], v[28:31], v[48:51], v[20:23]
	s_waitcnt vmcnt(1)
	v_mfma_f32_16x16x32_bf16 v[24:27], v[32:35], v[48:51], v[24:27]
	s_waitcnt vmcnt(0)
	v_mfma_f32_16x16x32_bf16 v[16:19], v[40:43], v[48:51], v[16:19]
	s_nop 1
	ds_write_b128 v11, v[12:15]
	s_nop 0
	ds_write_b128 v11, v[20:23] offset:1024
	s_nop 0
	ds_write_b128 v11, v[24:27] offset:2048
	s_nop 0
	ds_write_b128 v11, v[16:19] offset:3072
	s_waitcnt lgkmcnt(0)
	s_barrier
	s_cbranch_vccnz .LBB0_816
	v_add_u32_e32 v80, s6, v10
	v_ashrrev_i32_e32 v81, 31, v80
	v_lshl_add_u64 v[82:83], v[80:81], 2, v[6:7]
	global_load_dwordx4 v[12:15], v[82:83], off
	global_load_dwordx4 v[88:91], v[82:83], off offset:64
	global_load_dwordx4 v[92:95], v[82:83], off offset:128
	global_load_dwordx4 v[96:99], v[82:83], off offset:192
	ds_read_b128 v[16:19], v1
	ds_read_b128 v[20:23], v1 offset:1024
	ds_read_b128 v[24:27], v1 offset:4096
	ds_read_b128 v[28:31], v1 offset:5120
	ds_read_b128 v[32:35], v1 offset:8192
	ds_read_b128 v[36:39], v1 offset:9216
	ds_read_b128 v[40:43], v1 offset:12288
	ds_read_b128 v[44:47], v1 offset:13312
	ds_read_b128 v[48:51], v1 offset:16384
	ds_read_b128 v[52:55], v1 offset:17408
	ds_read_b128 v[56:59], v1 offset:20480
	ds_read_b128 v[60:63], v1 offset:21504
	ds_read_b128 v[64:67], v1 offset:24576
	ds_read_b128 v[68:71], v1 offset:25600
	ds_read_b128 v[72:75], v1 offset:28672
	ds_read_b128 v[76:79], v1 offset:29696
	s_waitcnt lgkmcnt(13)
	v_pk_add_f32 v[18:19], v[18:19], v[26:27]
	v_pk_add_f32 v[16:17], v[16:17], v[24:25]
	s_waitcnt lgkmcnt(11)
	v_pk_add_f32 v[18:19], v[18:19], v[34:35]
	v_pk_add_f32 v[16:17], v[16:17], v[32:33]
	s_waitcnt lgkmcnt(9)
	v_pk_add_f32 v[18:19], v[18:19], v[42:43]
	v_pk_add_f32 v[16:17], v[16:17], v[40:41]
	s_waitcnt lgkmcnt(7)
	v_pk_add_f32 v[18:19], v[18:19], v[50:51]
	v_pk_add_f32 v[16:17], v[16:17], v[48:49]
	s_waitcnt lgkmcnt(5)
	v_pk_add_f32 v[18:19], v[18:19], v[58:59]
	v_pk_add_f32 v[16:17], v[16:17], v[56:57]
	s_waitcnt lgkmcnt(3)
	v_pk_add_f32 v[18:19], v[18:19], v[66:67]
	v_pk_add_f32 v[16:17], v[16:17], v[64:65]
	s_waitcnt lgkmcnt(1)
	v_pk_add_f32 v[18:19], v[18:19], v[74:75]
	v_pk_add_f32 v[16:17], v[16:17], v[72:73]
	v_lshl_add_u64 v[84:85], v[80:81], 1, v[8:9]
	v_pk_add_f32 v[20:21], v[20:21], v[28:29]
	s_waitcnt vmcnt(3)
	v_pk_add_f32 v[14:15], v[18:19], v[14:15]
	v_pk_add_f32 v[12:13], v[16:17], v[12:13]
	v_bfe_u32 v18, v14, 16, 1
	v_bfe_u32 v16, v12, 16, 1
	v_bfe_u32 v17, v13, 16, 1
	v_bfe_u32 v19, v15, 16, 1
	v_add3_u32 v12, v12, v16, s8
	v_add3_u32 v14, v14, v18, s8
	v_add3_u32 v13, v13, v17, s8
	v_add3_u32 v15, v15, v19, s8
	v_lshrrev_b32_e32 v12, 16, v12
	v_lshrrev_b32_e32 v14, 16, v14
	v_and_or_b32 v12, v13, s9, v12
	v_and_or_b32 v13, v15, s9, v14
	global_store_dwordx2 v[84:85], v[12:13], off sc1
	v_pk_add_f32 v[18:19], v[22:23], v[30:31]
	v_pk_add_f32 v[20:21], v[20:21], v[36:37]
	v_pk_add_f32 v[18:19], v[18:19], v[38:39]
	v_pk_add_f32 v[20:21], v[20:21], v[44:45]
	v_pk_add_f32 v[18:19], v[18:19], v[46:47]
	v_pk_add_f32 v[20:21], v[20:21], v[52:53]
	v_pk_add_f32 v[18:19], v[18:19], v[54:55]
	v_pk_add_f32 v[20:21], v[20:21], v[60:61]
	v_pk_add_f32 v[18:19], v[18:19], v[62:63]
	v_pk_add_f32 v[20:21], v[20:21], v[68:69]
	v_pk_add_f32 v[18:19], v[18:19], v[70:71]
	s_waitcnt lgkmcnt(0)
	v_pk_add_f32 v[20:21], v[20:21], v[76:77]
	v_pk_add_f32 v[18:19], v[18:19], v[78:79]
	v_add_u32_e32 v16, 16, v80
	v_ashrrev_i32_e32 v17, 31, v16
	v_lshl_add_u64 v[16:17], v[16:17], 1, v[8:9]
	v_add_u32_e32 v84, 32, v80
	v_ashrrev_i32_e32 v85, 31, v84
	v_lshl_add_u64 v[84:85], v[84:85], 1, v[8:9]
	s_waitcnt vmcnt(3)
	v_pk_add_f32 v[14:15], v[18:19], v[90:91]
	v_pk_add_f32 v[12:13], v[20:21], v[88:89]
	v_bfe_u32 v20, v14, 16, 1
	v_bfe_u32 v18, v12, 16, 1
	v_bfe_u32 v19, v13, 16, 1
	v_bfe_u32 v21, v15, 16, 1
	v_add3_u32 v12, v12, v18, s8
	v_add3_u32 v14, v14, v20, s8
	v_add3_u32 v13, v13, v19, s8
	v_add3_u32 v15, v15, v21, s8
	v_lshrrev_b32_e32 v12, 16, v12
	v_lshrrev_b32_e32 v14, 16, v14
	v_and_or_b32 v12, v13, s9, v12
	v_and_or_b32 v13, v15, s9, v14
	global_store_dwordx2 v[16:17], v[12:13], off sc1
	ds_read_b128 v[16:19], v1 offset:2048
	ds_read_b128 v[20:23], v1 offset:3072
	ds_read_b128 v[24:27], v1 offset:6144
	ds_read_b128 v[28:31], v1 offset:7168
	ds_read_b128 v[32:35], v1 offset:10240
	ds_read_b128 v[36:39], v1 offset:11264
	ds_read_b128 v[40:43], v1 offset:14336
	ds_read_b128 v[44:47], v1 offset:15360
	ds_read_b128 v[48:51], v1 offset:18432
	ds_read_b128 v[52:55], v1 offset:19456
	ds_read_b128 v[56:59], v1 offset:22528
	ds_read_b128 v[60:63], v1 offset:23552
	ds_read_b128 v[64:67], v1 offset:26624
	ds_read_b128 v[68:71], v1 offset:27648
	ds_read_b128 v[72:75], v1 offset:30720
	ds_read_b128 v[76:79], v1 offset:31744
	s_waitcnt lgkmcnt(13)
	v_pk_add_f32 v[18:19], v[18:19], v[26:27]
	v_pk_add_f32 v[16:17], v[16:17], v[24:25]
	s_waitcnt lgkmcnt(11)
	v_pk_add_f32 v[18:19], v[18:19], v[34:35]
	v_pk_add_f32 v[16:17], v[16:17], v[32:33]
	s_waitcnt lgkmcnt(9)
	v_pk_add_f32 v[18:19], v[18:19], v[42:43]
	v_pk_add_f32 v[16:17], v[16:17], v[40:41]
	s_waitcnt lgkmcnt(7)
	v_pk_add_f32 v[18:19], v[18:19], v[50:51]
	v_pk_add_f32 v[16:17], v[16:17], v[48:49]
	s_waitcnt lgkmcnt(5)
	v_pk_add_f32 v[18:19], v[18:19], v[58:59]
	v_pk_add_f32 v[16:17], v[16:17], v[56:57]
	s_waitcnt lgkmcnt(3)
	v_pk_add_f32 v[18:19], v[18:19], v[66:67]
	v_pk_add_f32 v[16:17], v[16:17], v[64:65]
	s_waitcnt lgkmcnt(1)
	v_pk_add_f32 v[18:19], v[18:19], v[74:75]
	v_pk_add_f32 v[16:17], v[16:17], v[72:73]
	v_pk_add_f32 v[20:21], v[20:21], v[28:29]
	s_waitcnt vmcnt(3)
	v_pk_add_f32 v[14:15], v[18:19], v[94:95]
	v_pk_add_f32 v[12:13], v[16:17], v[92:93]
	v_bfe_u32 v18, v14, 16, 1
	v_bfe_u32 v16, v12, 16, 1
	v_bfe_u32 v17, v13, 16, 1
	v_bfe_u32 v19, v15, 16, 1
	v_add3_u32 v12, v12, v16, s8
	v_add3_u32 v14, v14, v18, s8
	v_add3_u32 v13, v13, v17, s8
	v_add3_u32 v15, v15, v19, s8
	v_lshrrev_b32_e32 v12, 16, v12
	v_lshrrev_b32_e32 v14, 16, v14
	v_and_or_b32 v12, v13, s9, v12
	v_and_or_b32 v13, v15, s9, v14
	global_store_dwordx2 v[84:85], v[12:13], off sc1
	v_pk_add_f32 v[18:19], v[22:23], v[30:31]
	v_pk_add_f32 v[20:21], v[20:21], v[36:37]
	v_pk_add_f32 v[18:19], v[18:19], v[38:39]
	v_pk_add_f32 v[20:21], v[20:21], v[44:45]
	v_pk_add_f32 v[18:19], v[18:19], v[46:47]
	v_pk_add_f32 v[20:21], v[20:21], v[52:53]
	v_pk_add_f32 v[18:19], v[18:19], v[54:55]
	v_pk_add_f32 v[20:21], v[20:21], v[60:61]
	v_pk_add_f32 v[18:19], v[18:19], v[62:63]
	v_pk_add_f32 v[20:21], v[20:21], v[68:69]
	v_pk_add_f32 v[18:19], v[18:19], v[70:71]
	s_waitcnt lgkmcnt(0)
	v_pk_add_f32 v[20:21], v[20:21], v[76:77]
	v_pk_add_f32 v[18:19], v[18:19], v[78:79]
	v_add_u32_e32 v16, 48, v80
	v_ashrrev_i32_e32 v17, 31, v16
	s_waitcnt vmcnt(3)
	v_pk_add_f32 v[14:15], v[18:19], v[98:99]
	v_pk_add_f32 v[12:13], v[20:21], v[96:97]
	v_bfe_u32 v20, v14, 16, 1
	v_bfe_u32 v18, v12, 16, 1
	v_bfe_u32 v19, v13, 16, 1
	v_bfe_u32 v21, v15, 16, 1
	v_add3_u32 v12, v12, v18, s8
	v_add3_u32 v14, v14, v20, s8
	v_add3_u32 v13, v13, v19, s8
	v_add3_u32 v15, v15, v21, s8
	v_lshrrev_b32_e32 v12, 16, v12
	v_lshrrev_b32_e32 v14, 16, v14
	v_and_or_b32 v12, v13, s9, v12
	v_and_or_b32 v13, v15, s9, v14
	v_lshl_add_u64 v[14:15], v[16:17], 1, v[8:9]
	global_store_dwordx2 v[14:15], v[12:13], off sc1
	s_branch .LBB0_816

.LBB0_839:
	v_readlane_b32 s44, v253, 2
	v_readlane_b32 s45, v253, 3
	v_lshl_or_b32 v155, s41, 8, v153
	v_lshl_add_u32 v156, s20, 8, v1
	v_lshlrev_b32_e32 v155, 2, v155
	v_lshl_add_u32 v157, v156, 12, v155
	v_mov_b32_e32 v146, v157
	v_add_u32_e32 v147, 0x10000, v157
	v_add_u32_e32 v148, 0x20000, v157
	v_add_u32_e32 v149, 0x30000, v157
	v_add_u32_e32 v150, 0x80000, v157
	v_add_u32_e32 v151, 0x90000, v157
	v_add_u32_e32 v152, 0xa0000, v157
	v_add_u32_e32 v154, 0xb0000, v157
	global_load_dwordx4 v[160:163], v146, s[44:45] nt
	global_load_dwordx4 v[164:167], v146, s[44:45] offset:16 nt
	global_load_dwordx4 v[168:171], v146, s[44:45] offset:512 nt
	global_load_dwordx4 v[172:175], v146, s[44:45] offset:528 nt
	global_load_dwordx4 v[176:179], v147, s[44:45] nt
	global_load_dwordx4 v[180:183], v147, s[44:45] offset:16 nt
	global_load_dwordx4 v[184:187], v147, s[44:45] offset:512 nt
	global_load_dwordx4 v[188:191], v147, s[44:45] offset:528 nt
	global_load_dwordx4 v[194:197], v148, s[44:45] nt
	global_load_dwordx4 v[198:201], v148, s[44:45] offset:16 nt
	global_load_dwordx4 v[202:205], v148, s[44:45] offset:512 nt
	global_load_dwordx4 v[210:213], v148, s[44:45] offset:528 nt
	global_load_dwordx4 v[214:217], v149, s[44:45] nt
	global_load_dwordx4 v[218:221], v149, s[44:45] offset:16 nt
	global_load_dwordx4 v[230:233], v149, s[44:45] offset:512 nt
	global_load_dwordx4 v[234:237], v149, s[44:45] offset:528 nt
	s_andn2_b64 vcc, exec, s[4:5]
	s_mov_b64 s[4:5], -1
	v_readlane_b32 s46, v253, 4
	v_readlane_b32 s47, v253, 5
	v_readlane_b32 s48, v253, 6
	v_readlane_b32 s49, v253, 7
	v_readlane_b32 s50, v253, 8
	v_readlane_b32 s51, v253, 9
	v_readlane_b32 s52, v253, 10
	v_readlane_b32 s53, v253, 11
	v_readlane_b32 s54, v253, 12
	v_readlane_b32 s55, v253, 13
	v_readlane_b32 s56, v253, 14
	v_readlane_b32 s57, v253, 15
	v_readlane_b32 s58, v253, 16
	v_readlane_b32 s59, v253, 17
	s_waitcnt vmcnt(8)
	v_pk_add_f32 v[126:127], v[126:127], v[160:161]
	v_pk_add_f32 v[128:129], v[128:129], v[162:163]
	v_pk_add_f32 v[122:123], v[122:123], v[164:165]
	v_pk_add_f32 v[124:125], v[124:125], v[166:167]
	v_pk_add_f32 v[110:111], v[110:111], v[168:169]
	v_pk_add_f32 v[112:113], v[112:113], v[170:171]
	v_pk_add_f32 v[106:107], v[106:107], v[172:173]
	v_pk_add_f32 v[108:109], v[108:109], v[174:175]
	v_pk_add_f32 v[118:119], v[118:119], v[176:177]
	v_pk_add_f32 v[120:121], v[120:121], v[178:179]
	v_pk_add_f32 v[114:115], v[114:115], v[180:181]
	v_pk_add_f32 v[116:117], v[116:117], v[182:183]
	v_pk_add_f32 v[102:103], v[102:103], v[184:185]
	v_pk_add_f32 v[104:105], v[104:105], v[186:187]
	v_pk_add_f32 v[98:99], v[98:99], v[188:189]
	v_pk_add_f32 v[100:101], v[100:101], v[190:191]
	global_load_dwordx4 v[160:163], v150, s[44:45] nt
	global_load_dwordx4 v[164:167], v150, s[44:45] offset:16 nt
	global_load_dwordx4 v[168:171], v150, s[44:45] offset:512 nt
	global_load_dwordx4 v[172:175], v150, s[44:45] offset:528 nt
	global_load_dwordx4 v[176:179], v151, s[44:45] nt
	global_load_dwordx4 v[180:183], v151, s[44:45] offset:16 nt
	global_load_dwordx4 v[184:187], v151, s[44:45] offset:512 nt
	global_load_dwordx4 v[188:191], v151, s[44:45] offset:528 nt
	v_lshrrev_b32_e32 v156, 1, v146
	v_cvt_pk_bf16_f32 v126, v126, v127
	v_cvt_pk_bf16_f32 v127, v128, v129
	v_cvt_pk_bf16_f32 v128, v122, v123
	v_cvt_pk_bf16_f32 v129, v124, v125
	global_store_dwordx4 v156, v[126:129], s[82:83] sc1
	v_cvt_pk_bf16_f32 v110, v110, v111
	v_cvt_pk_bf16_f32 v111, v112, v113
	v_cvt_pk_bf16_f32 v112, v106, v107
	v_cvt_pk_bf16_f32 v113, v108, v109
	global_store_dwordx4 v156, v[110:113], s[82:83] offset:256 sc1
	v_lshrrev_b32_e32 v155, 1, v147
	v_cvt_pk_bf16_f32 v118, v118, v119
	v_cvt_pk_bf16_f32 v119, v120, v121
	v_cvt_pk_bf16_f32 v120, v114, v115
	v_cvt_pk_bf16_f32 v121, v116, v117
	global_store_dwordx4 v155, v[118:121], s[82:83] sc1
	v_cvt_pk_bf16_f32 v102, v102, v103
	v_cvt_pk_bf16_f32 v103, v104, v105
	v_cvt_pk_bf16_f32 v104, v98, v99
	v_cvt_pk_bf16_f32 v105, v100, v101
	global_store_dwordx4 v155, v[102:105], s[82:83] offset:256 sc1
	s_waitcnt vmcnt(12)
	v_pk_add_f32 v[94:95], v[94:95], v[194:195]
	v_pk_add_f32 v[96:97], v[96:97], v[196:197]
	v_pk_add_f32 v[90:91], v[90:91], v[198:199]
	v_pk_add_f32 v[92:93], v[92:93], v[200:201]
	v_pk_add_f32 v[78:79], v[78:79], v[202:203]
	v_pk_add_f32 v[80:81], v[80:81], v[204:205]
	v_pk_add_f32 v[74:75], v[74:75], v[210:211]
	v_pk_add_f32 v[76:77], v[76:77], v[212:213]
	v_pk_add_f32 v[86:87], v[86:87], v[214:215]
	v_pk_add_f32 v[88:89], v[88:89], v[216:217]
	v_pk_add_f32 v[82:83], v[82:83], v[218:219]
	v_pk_add_f32 v[84:85], v[84:85], v[220:221]
	v_pk_add_f32 v[70:71], v[70:71], v[230:231]
	v_pk_add_f32 v[72:73], v[72:73], v[232:233]
	v_pk_add_f32 v[66:67], v[66:67], v[234:235]
	v_pk_add_f32 v[68:69], v[68:69], v[236:237]
	global_load_dwordx4 v[194:197], v152, s[44:45] nt
	global_load_dwordx4 v[198:201], v152, s[44:45] offset:16 nt
	global_load_dwordx4 v[202:205], v152, s[44:45] offset:512 nt
	global_load_dwordx4 v[210:213], v152, s[44:45] offset:528 nt
	global_load_dwordx4 v[214:217], v154, s[44:45] nt
	global_load_dwordx4 v[218:221], v154, s[44:45] offset:16 nt
	global_load_dwordx4 v[230:233], v154, s[44:45] offset:512 nt
	global_load_dwordx4 v[234:237], v154, s[44:45] offset:528 nt
	v_lshrrev_b32_e32 v156, 1, v148
	v_cvt_pk_bf16_f32 v94, v94, v95
	v_cvt_pk_bf16_f32 v95, v96, v97
	v_cvt_pk_bf16_f32 v96, v90, v91
	v_cvt_pk_bf16_f32 v97, v92, v93
	global_store_dwordx4 v156, v[94:97], s[82:83] sc1
	v_cvt_pk_bf16_f32 v78, v78, v79
	v_cvt_pk_bf16_f32 v79, v80, v81
	v_cvt_pk_bf16_f32 v80, v74, v75
	v_cvt_pk_bf16_f32 v81, v76, v77
	global_store_dwordx4 v156, v[78:81], s[82:83] offset:256 sc1
	v_lshrrev_b32_e32 v155, 1, v149
	v_cvt_pk_bf16_f32 v86, v86, v87
	v_cvt_pk_bf16_f32 v87, v88, v89
	v_cvt_pk_bf16_f32 v88, v82, v83
	v_cvt_pk_bf16_f32 v89, v84, v85
	global_store_dwordx4 v155, v[86:89], s[82:83] sc1
	v_cvt_pk_bf16_f32 v70, v70, v71
	v_cvt_pk_bf16_f32 v71, v72, v73
	v_cvt_pk_bf16_f32 v72, v66, v67
	v_cvt_pk_bf16_f32 v73, v68, v69
	global_store_dwordx4 v155, v[70:73], s[82:83] offset:256 sc1
	s_waitcnt vmcnt(16)
	v_pk_add_f32 v[62:63], v[62:63], v[160:161]
	v_pk_add_f32 v[64:65], v[64:65], v[162:163]
	v_pk_add_f32 v[58:59], v[58:59], v[164:165]
	v_pk_add_f32 v[60:61], v[60:61], v[166:167]
	v_pk_add_f32 v[46:47], v[46:47], v[168:169]
	v_pk_add_f32 v[48:49], v[48:49], v[170:171]
	v_pk_add_f32 v[42:43], v[42:43], v[172:173]
	v_pk_add_f32 v[44:45], v[44:45], v[174:175]
	v_pk_add_f32 v[54:55], v[54:55], v[176:177]
	v_pk_add_f32 v[56:57], v[56:57], v[178:179]
	v_pk_add_f32 v[50:51], v[50:51], v[180:181]
	v_pk_add_f32 v[52:53], v[52:53], v[182:183]
	v_pk_add_f32 v[38:39], v[38:39], v[184:185]
	v_pk_add_f32 v[40:41], v[40:41], v[186:187]
	v_pk_add_f32 v[34:35], v[34:35], v[188:189]
	v_pk_add_f32 v[36:37], v[36:37], v[190:191]
	v_lshrrev_b32_e32 v156, 1, v150
	v_cvt_pk_bf16_f32 v62, v62, v63
	v_cvt_pk_bf16_f32 v63, v64, v65
	v_cvt_pk_bf16_f32 v64, v58, v59
	v_cvt_pk_bf16_f32 v65, v60, v61
	global_store_dwordx4 v156, v[62:65], s[82:83] sc1
	v_cvt_pk_bf16_f32 v46, v46, v47
	v_cvt_pk_bf16_f32 v47, v48, v49
	v_cvt_pk_bf16_f32 v48, v42, v43
	v_cvt_pk_bf16_f32 v49, v44, v45
	global_store_dwordx4 v156, v[46:49], s[82:83] offset:256 sc1
	v_lshrrev_b32_e32 v155, 1, v151
	v_cvt_pk_bf16_f32 v54, v54, v55
	v_cvt_pk_bf16_f32 v55, v56, v57
	v_cvt_pk_bf16_f32 v56, v50, v51
	v_cvt_pk_bf16_f32 v57, v52, v53
	global_store_dwordx4 v155, v[54:57], s[82:83] sc1
	v_cvt_pk_bf16_f32 v38, v38, v39
	v_cvt_pk_bf16_f32 v39, v40, v41
	v_cvt_pk_bf16_f32 v40, v34, v35
	v_cvt_pk_bf16_f32 v41, v36, v37
	global_store_dwordx4 v155, v[38:41], s[82:83] offset:256 sc1
	s_waitcnt vmcnt(8)
	v_pk_add_f32 v[30:31], v[30:31], v[194:195]
	v_pk_add_f32 v[32:33], v[32:33], v[196:197]
	v_pk_add_f32 v[26:27], v[26:27], v[198:199]
	v_pk_add_f32 v[28:29], v[28:29], v[200:201]
	v_pk_add_f32 v[14:15], v[14:15], v[202:203]
	v_pk_add_f32 v[16:17], v[16:17], v[204:205]
	v_pk_add_f32 v[10:11], v[10:11], v[210:211]
	v_pk_add_f32 v[12:13], v[12:13], v[212:213]
	v_pk_add_f32 v[22:23], v[22:23], v[214:215]
	v_pk_add_f32 v[24:25], v[24:25], v[216:217]
	v_pk_add_f32 v[18:19], v[18:19], v[218:219]
	v_pk_add_f32 v[20:21], v[20:21], v[220:221]
	v_pk_add_f32 v[6:7], v[6:7], v[230:231]
	v_pk_add_f32 v[8:9], v[8:9], v[232:233]
	v_pk_add_f32 v[2:3], v[2:3], v[234:235]
	v_pk_add_f32 v[4:5], v[4:5], v[236:237]
	v_lshrrev_b32_e32 v156, 1, v152
	v_cvt_pk_bf16_f32 v30, v30, v31
	v_cvt_pk_bf16_f32 v31, v32, v33
	v_cvt_pk_bf16_f32 v32, v26, v27
	v_cvt_pk_bf16_f32 v33, v28, v29
	global_store_dwordx4 v156, v[30:33], s[82:83] sc1
	v_cvt_pk_bf16_f32 v14, v14, v15
	v_cvt_pk_bf16_f32 v15, v16, v17
	v_cvt_pk_bf16_f32 v16, v10, v11
	v_cvt_pk_bf16_f32 v17, v12, v13
	global_store_dwordx4 v156, v[14:17], s[82:83] offset:256 sc1
	v_lshrrev_b32_e32 v155, 1, v154
	v_cvt_pk_bf16_f32 v22, v22, v23
	v_cvt_pk_bf16_f32 v23, v24, v25
	v_cvt_pk_bf16_f32 v24, v18, v19
	v_cvt_pk_bf16_f32 v25, v20, v21
	global_store_dwordx4 v155, v[22:25], s[82:83] sc1
	v_cvt_pk_bf16_f32 v6, v6, v7
	v_cvt_pk_bf16_f32 v7, v8, v9
	v_cvt_pk_bf16_f32 v8, v2, v3
	v_cvt_pk_bf16_f32 v9, v4, v5
	global_store_dwordx4 v155, v[6:9], s[82:83] offset:256 sc1
	s_cbranch_vccnz .LBB0_828
	s_andn2_b64 vcc, exec, s[6:7]
	s_cbranch_vccnz .LBB0_827
	s_barrier
	s_branch .LBB0_827
